# v59 + indexer pair-sync spin loops back off with s_sleep 1
# speedup vs baseline: 1.0080x; 1.0011x over previous
.LBB0_1436:
	v_mov_b32_e32 v149, s63
	s_sleep 1
	ds_read_b32 v149, v149 offset:8
	s_waitcnt lgkmcnt(0)
	v_cmp_ne_u32_e32 vcc, 1, v149
	s_cbranch_vccnz .LBB0_1436

.LBB0_1464:
	v_mov_b32_e32 v152, s63
	s_sleep 1
	ds_read_b32 v152, v152
	s_waitcnt lgkmcnt(0)
	v_cmp_ne_u32_e32 vcc, 2, v152
	s_cbranch_vccnz .LBB0_1464

.LBB0_1711:
	v_mov_b32_e32 v154, s29
	s_sleep 1
	ds_read_b32 v154, v154
	s_waitcnt lgkmcnt(0)
	v_cmp_ne_u32_sdwa s[58:59], v154, s90 src0_sel:WORD_1 src1_sel:DWORD
	s_and_b64 vcc, exec, s[58:59]
	s_cbranch_vccnz .LBB0_1711

.LBB0_1814:
	v_mov_b32_e32 v150, s58
	s_sleep 1
	ds_read_b32 v150, v150
	s_waitcnt lgkmcnt(0)
	v_cmp_eq_u32_sdwa s[60:61], v150, s29 src0_sel:WORD_1 src1_sel:DWORD
	s_and_b64 vcc, exec, s[60:61]
	s_cbranch_vccz .LBB0_1814
